# baseline (speedup 1.0000x reference)
_Z11attn_kernelPKfS0_S0_PKcS2_PKDv4_jS0_S0_S0_S0_Pf:
	s_load_dwordx8 s[4:11], s[0:1], 0x0
	s_load_dwordx8 s[12:19], s[0:1], 0x20
	v_readfirstlane_b32 s20, v0
	s_bfe_u32 s28, s2, 0x10002
	s_lshr_b32 s29, s20, 6
	s_lshr_b32 s3, s20, 8
	s_bfe_u32 s30, s20, 0x20006
	s_lshr_b32 s31, s2, 3
	s_lshl_b32 s24, s28, 18
	s_waitcnt lgkmcnt(0)
	s_add_u32 s20, s10, s24
	s_addc_u32 s10, s11, 0
	s_and_b32 s21, s10, 0xffff
	s_add_u32 s24, s12, s24
	s_addc_u32 s10, s13, 0
	v_and_b32_e32 v1, 63, v0
	s_and_b32 s25, s10, 0xffff
	s_lshl_b32 s10, s30, 10
	s_lshl_b32 s38, s3, 12
	v_lshlrev_b32_e32 v2, 4, v1
	s_or_b32 s35, s10, s38
	v_lshl_or_b32 v2, s3, 17, v2
	s_cmp_lg_u32 0, -1
	v_or_b32_e32 v174, s10, v2
	s_cselect_b32 s10, 0, 0
	s_mov_b32 s36, 0
	s_mov_b32 s23, 0x20000
	s_mov_b32 s22, 0x40000
	s_add_i32 s33, s35, s10
	s_mov_b32 m0, s33
	s_nop 0
	buffer_load_dwordx4 v174, s[20:23], s36 offen lds
	s_mov_b32 s26, s22
	s_mov_b32 s27, s23
	s_add_i32 s34, s33, 0xc000
	s_mov_b32 m0, s34
	s_nop 0
	buffer_load_dwordx4 v174, s[24:27], s36 offen lds
	s_add_i32 s10, s33, 0x4000
	s_movk_i32 s37, 0x1000
	s_mov_b32 m0, s10
	s_nop 0
	buffer_load_dwordx4 v174, s[20:23], s37 offen lds
	s_add_i32 s10, s33, 0x8000
	s_movk_i32 s11, 0x2000
	s_mov_b32 m0, s10
	s_nop 0
	buffer_load_dwordx4 v174, s[20:23], s11 offen lds
	s_lshl_b32 s10, s2, 7
	s_and_b32 s10, s10, 0x380
	s_lshl_b32 s11, s31, 2
	s_add_i32 s10, s10, s11
	s_or_b32 s10, s30, s10
	v_and_b32_e32 v172, 31, v0
	v_lshl_or_b32 v140, s10, 7, v1
	v_mov_b32_e32 v141, 0
	v_lshl_add_u64 v[6:7], v[140:141], 4, s[14:15]
	v_ashrrev_i32_e32 v9, 31, v140
	v_mov_b32_e32 v8, v140
	v_lshl_or_b32 v140, s10, 5, v172
	v_lshlrev_b64 v[4:5], 2, v[140:141]
	v_lshl_add_u64 v[2:3], s[16:17], 0, v[4:5]
	global_load_dword v2, v[2:3], off
	v_lshl_add_u64 v[8:9], v[8:9], 4, s[14:15]
	global_load_dwordx4 v[116:119], v[6:7], off
	global_load_dwordx4 v[120:123], v[8:9], off offset:1024
	s_load_dwordx4 s[12:15], s[0:1], 0x40
	s_load_dwordx2 s[10:11], s[0:1], 0x50
	v_lshlrev_b32_e32 v173, 2, v1
	v_lshl_or_b32 v3, s28, 11, v173
	s_waitcnt lgkmcnt(0)
	global_load_dword v44, v3, s[14:15] offset:256
	global_load_dword v45, v3, s[14:15]
	v_bfe_u32 v175, v0, 5, 1
	v_lshlrev_b32_e32 v0, 11, v175
	v_lshlrev_b32_e32 v3, 4, v172
	s_add_i32 s0, s38, 0
	v_lshl_add_u64 v[4:5], s[12:13], 0, v[4:5]
	v_add3_u32 v176, s0, v0, v3
	global_load_dword v0, v[4:5], off
	v_lshrrev_b32_e32 v124, 2, v1
	v_lshrrev_b32_e32 v125, 4, v1
	v_xor_b32_e32 v124, v124, v125
	v_and_b32_e32 v124, 1, v124
	v_add_u32_e32 v124, -1, v124
	v_and_b32_e32 v124, 0x38383838, v124
	v_mov_b32_e32 v200, 0
	v_mov_b32_e32 v201, 0
	v_mov_b32_e32 v202, 0
	v_mov_b32_e32 v203, 0
	v_mov_b32_e32 v204, 0
	v_mov_b32_e32 v125, v124
	v_mov_b32_e32 v126, v124
	v_mov_b32_e32 v127, v124
	v_mov_b32_e32 v128, v124
	v_mov_b32_e32 v129, v124
	v_mov_b32_e32 v130, v124
	v_mov_b32_e32 v131, v124
	v_mov_b32_e32 v140, 0x7f7f7f7f
	s_mov_b32 s0, 0xf800000
	s_movk_i32 s15, 0x3000
	s_mov_b32 s12, 1
	s_movk_i32 s14, 0x4000
	s_mov_b32 s13, 0x8000
	v_mov_b64_e32 v[132:133], 0
	v_mov_b64_e32 v[134:135], 0
	v_mov_b64_e32 v[136:137], 0
	v_mov_b64_e32 v[138:139], 0
	s_waitcnt vmcnt(5)
	v_mov_b32_e32 v4, v2
	v_mov_b32_e32 v5, v2
	v_mov_b32_e32 v6, v2
	v_mov_b32_e32 v7, v2
	v_mov_b32_e32 v8, v2
	v_mov_b32_e32 v9, v2
	v_mov_b32_e32 v10, v2
	v_mov_b32_e32 v11, v2
	v_mov_b32_e32 v12, v2
	v_mov_b32_e32 v13, v2
	v_mov_b32_e32 v14, v2
	v_mov_b32_e32 v15, v2
	v_mov_b32_e32 v16, v2
	v_mov_b32_e32 v17, v2
	v_mov_b32_e32 v3, v2
	v_mov_b64_e32 v[18:19], v[16:17]
	v_mov_b64_e32 v[16:17], v[14:15]
	v_mov_b64_e32 v[14:15], v[12:13]
	v_mov_b64_e32 v[12:13], v[10:11]
	v_mov_b64_e32 v[10:11], v[8:9]
	v_mov_b64_e32 v[8:9], v[6:7]
	v_mov_b64_e32 v[6:7], v[4:5]
	v_mov_b64_e32 v[4:5], v[2:3]
	s_waitcnt vmcnt(0) lgkmcnt(0)
	s_barrier
	ds_read_b128 v[24:27], v176 offset:1024
	ds_read_b128 v[20:23], v176
	ds_read_b128 v[36:39], v176 offset:512
	ds_read_b128 v[40:43], v176 offset:1536
	ds_read_b128 v[84:87], v176 offset:16384
	ds_read_b128 v[92:95], v176 offset:16896
	ds_read_b128 v[88:91], v176 offset:17408
	ds_read_b128 v[96:99], v176 offset:17920
	s_waitcnt vmcnt(3) lgkmcnt(6)
	v_mfma_f32_32x32x64_f8f6f4 v[20:35], v[20:27], v[116:123], v[4:19]
	s_waitcnt vmcnt(2)
	v_max_f32_e32 v3, v44, v44
	s_waitcnt vmcnt(1)
	v_max_f32_e32 v44, v45, v45
	v_max_f32_e32 v44, v44, v3
	s_nop 1
	v_max_f32_dpp v44, v44, v44 quad_perm:[1,0,3,2] row_mask:0xf bank_mask:0xf
	s_nop 1
	v_max_f32_dpp v44, v44, v44 quad_perm:[2,3,0,1] row_mask:0xf bank_mask:0xf
	s_nop 1
	v_max_f32_dpp v44, v44, v44 row_half_mirror row_mask:0xf bank_mask:0xf
	s_nop 1
	v_max_f32_dpp v44, v44, v44 row_mirror row_mask:0xf bank_mask:0xf
	s_nop 1
	v_max_f32_dpp v44, v44, v44 row_bcast:15 row_mask:0xa bank_mask:0xf
	s_nop 1
	v_max_f32_dpp v44, v44, v44 row_bcast:31 row_mask:0xc bank_mask:0xf
	s_nop 1
	v_readlane_b32 s47, v44, 63
	s_waitcnt vmcnt(0) lgkmcnt(0)
	s_barrier
	v_mfma_f32_32x32x64_f8f6f4 v[4:19], v[36:43], v[116:123], v[4:19]
	s_mov_b32 m0, s33
	s_nop 0
	buffer_load_dwordx4 v174, s[20:23], s15 offen lds
	s_add_i32 s15, s34, 0x4000
	s_mov_b32 m0, s15
	s_nop 0
	buffer_load_dwordx4 v174, s[24:27], s37 offen lds
	s_nop 1
	v_max_f32_e32 v3, v21, v21
	v_max_f32_e32 v36, v20, v20
	v_max_f32_e32 v3, v36, v3
	s_nop 7
	v_max3_f32 v37, v22, v23, v5
	v_max3_f32 v36, v37, v26, v27
	v_max3_f32 v3, v3, v4, v6
	v_max3_f32 v3, v3, v7, v24
	v_max3_f32 v36, v36, v10, v11
	v_max3_f32 v3, v3, v25, v8
	v_max3_f32 v36, v36, v30, v31
	v_max3_f32 v3, v3, v9, v28
	v_max3_f32 v36, v36, v14, v15
	v_max3_f32 v3, v3, v29, v12
	v_max3_f32 v36, v36, v34, v35
	v_max3_f32 v3, v3, v13, v32
	v_max3_f32 v36, v36, v18, v19
	v_max3_f32 v3, v3, v33, v16
	v_max3_f32 v3, v3, v17, v36
	v_mov_b32_e32 v36, v3
	s_nop 1
	v_permlane32_swap_b32_e32 v3, v36
	v_max_f32_e32 v36, v36, v36
	v_max_f32_e32 v3, v3, v3
	v_max_f32_e32 v3, v3, v36
	v_sub_f32_e32 v36, 0xc0400000, v3
	v_pk_add_f32 v[20:21], v[36:37], v[20:21] op_sel_hi:[0,1]
	v_pk_add_f32 v[22:23], v[36:37], v[22:23] op_sel_hi:[0,1]
	v_pk_add_f32 v[24:25], v[36:37], v[24:25] op_sel_hi:[0,1]
	v_pk_add_f32 v[26:27], v[36:37], v[26:27] op_sel_hi:[0,1]
	v_pk_add_f32 v[28:29], v[36:37], v[28:29] op_sel_hi:[0,1]
	v_mov_b32_e32 v37, s47
	v_mul_f32_e32 v38, 0x4f800000, v37
	v_cmp_gt_f32_e32 vcc, s0, v37
	v_pk_add_f32 v[30:31], v[36:37], v[30:31] op_sel_hi:[0,1]
	v_cndmask_b32_e32 v37, v37, v38, vcc
	v_sqrt_f32_e32 v38, v37
	v_pk_add_f32 v[32:33], v[36:37], v[32:33] op_sel_hi:[0,1]
	v_pk_add_f32 v[34:35], v[36:37], v[34:35] op_sel_hi:[0,1]
	v_pk_add_f32 v[4:5], v[36:37], v[4:5] op_sel_hi:[0,1]
	v_pk_add_f32 v[6:7], v[36:37], v[6:7] op_sel_hi:[0,1]
	v_pk_add_f32 v[8:9], v[36:37], v[8:9] op_sel_hi:[0,1]
	v_pk_add_f32 v[10:11], v[36:37], v[10:11] op_sel_hi:[0,1]
	v_pk_add_f32 v[12:13], v[36:37], v[12:13] op_sel_hi:[0,1]
	v_pk_add_f32 v[14:15], v[36:37], v[14:15] op_sel_hi:[0,1]
	v_pk_add_f32 v[16:17], v[36:37], v[16:17] op_sel_hi:[0,1]
	v_pk_add_f32 v[18:19], v[36:37], v[18:19] op_sel_hi:[0,1]
	v_add_u32_e32 v36, -1, v38
	v_fma_f32 v39, -v36, v38, v37
	v_cmp_ge_f32_e64 s[0:1], 0, v39
	v_add_u32_e32 v39, 1, v38
	v_exp_f32_e32 v161, v20
	v_cndmask_b32_e64 v36, v38, v36, s[0:1]
	v_fma_f32 v38, -v39, v38, v37
	v_cmp_lt_f32_e64 s[0:1], 0, v38
	v_exp_f32_e32 v100, v4
	v_exp_f32_e32 v163, v21
	v_cndmask_b32_e64 v36, v36, v39, s[0:1]
	v_mul_f32_e32 v38, 0x37800000, v36
	v_cndmask_b32_e32 v36, v36, v38, vcc
	v_mov_b32_e32 v38, 0x260
	v_cmp_class_f32_e32 vcc, v37, v38
	s_mov_b32 s0, 0x42700000
	v_exp_f32_e32 v148, v5
	v_cndmask_b32_e32 v36, v36, v37, vcc
	s_waitcnt vmcnt(0)
	v_mul_f32_e32 v0, v36, v0
	v_mul_f32_e32 v0, 0x3f91eb85, v0
	v_exp_f32_e32 v162, v22
	v_exp_f32_e32 v101, v6
	v_exp_f32_e32 v164, v23
	v_exp_f32_e32 v102, v7
	v_exp_f32_e32 v150, v24
	v_exp_f32_e32 v143, v8
	v_exp_f32_e32 v154, v25
	v_exp_f32_e32 v146, v9
	v_exp_f32_e32 v152, v26
	v_exp_f32_e32 v145, v10
	v_exp_f32_e32 v157, v27
	v_exp_f32_e32 v147, v11
	v_exp_f32_e32 v149, v28
	v_exp_f32_e32 v69, v12
	v_exp_f32_e32 v153, v29
	v_exp_f32_e32 v109, v13
	v_exp_f32_e32 v151, v30
	v_exp_f32_e32 v108, v14
	v_exp_f32_e32 v156, v31
	v_exp_f32_e32 v142, v15
	v_exp_f32_e32 v155, v32
	v_exp_f32_e32 v110, v16
	v_exp_f32_e32 v159, v33
	v_exp_f32_e32 v144, v17
	v_exp_f32_e32 v158, v34
	v_exp_f32_e32 v111, v18
	v_exp_f32_e32 v160, v35
	v_exp_f32_e32 v114, v19
	v_cmp_nge_f32_e64 s[0:1], s0, v0
	v_sub_f32_e32 v0, v2, v3
	v_add_f32_e32 v36, 0xc0400000, v0
	v_mov_b32_e32 v37, v36
	v_mov_b64_e32 v[38:39], v[36:37]
	v_mov_b64_e32 v[40:41], v[36:37]
	v_mov_b64_e32 v[42:43], v[36:37]
	v_mov_b64_e32 v[44:45], v[36:37]
	v_mov_b64_e32 v[46:47], v[36:37]
	v_mov_b64_e32 v[48:49], v[36:37]
	v_mov_b64_e32 v[50:51], v[36:37]
	v_mov_b64_e32 v[4:5], 0
	v_mov_b64_e32 v[6:7], 0
	v_mov_b64_e32 v[8:9], 0
	v_mov_b64_e32 v[10:11], 0
	v_mov_b64_e32 v[12:13], 0
	v_mov_b64_e32 v[14:15], 0
	v_mov_b64_e32 v[16:17], 0
	v_mov_b64_e32 v[18:19], 0
	v_mov_b64_e32 v[20:21], 0
	v_mov_b64_e32 v[22:23], 0
	v_mov_b64_e32 v[24:25], 0
	v_mov_b64_e32 v[26:27], 0
	v_mov_b64_e32 v[28:29], 0
	v_mov_b64_e32 v[30:31], 0
	v_mov_b64_e32 v[32:33], 0
	v_mov_b64_e32 v[34:35], 0
	v_mov_b32_e32 v0, v141

.LBB1_11:
	s_lshl_b32 s0, s30, 5
	s_lshl_b32 s1, s31, 7
	s_and_b32 s13, s2, 3
	s_or_b32 s14, s0, s1
	s_lshl_b32 s4, s28, 7
	s_lshl_b32 s5, s31, 2
	s_add_i32 s4, s4, s5
	s_add_i32 s4, s4, s30
	s_lshl_b32 s4, s4, 1
	s_add_i32 s4, s4, s3
	s_lshl_b32 s4, s4, 12
	s_add_u32 s4, s18, s4
	s_addc_u32 s5, s19, 0
	v_lshlrev_b32_e32 v0, 2, v173
	s_lshl_b32 s0, s3, 5
	s_lshl_b32 s12, s13, 6
	s_mov_b32 s1, 0
	s_mov_b32 s15, 0
	global_load_dwordx4 v[124:127], v0, s[4:5]
	global_load_dwordx4 v[128:131], v0, s[4:5] offset:1024
	global_load_dwordx4 v[132:135], v0, s[4:5] offset:2048
	global_load_dwordx4 v[136:139], v0, s[4:5] offset:3072
	s_lshl_b64 s[2:3], s[14:15], 2
	v_mov_b32_e32 v37, 0
	v_lshlrev_b32_e32 v36, 2, v172
	v_lshlrev_b32_e32 v122, 16, v175
	v_mov_b32_e32 v123, 0
	s_mul_i32 s4, s29, 0x2200
	s_add_i32 s4, s4, 0
	v_mov_b32_e32 v8, v141
	v_add_u32_e32 v9, s4, v173
	s_xor_b32 s4, s29, 4
	v_permlane32_swap_b32_e32 v141, v8
	s_mulk_i32 s4, 0x2200
	v_add_f32_e32 v8, v141, v8
	s_add_i32 s4, s4, 0
	ds_write2st64_b32 v9, v146, v8 offset1:1
	ds_write2st64_b32 v9, v86, v87 offset0:2 offset1:3
	ds_write2st64_b32 v9, v70, v71 offset0:18 offset1:19
	ds_write2st64_b32 v9, v88, v89 offset0:4 offset1:5
	ds_write2st64_b32 v9, v72, v73 offset0:20 offset1:21
	ds_write2st64_b32 v9, v90, v91 offset0:6 offset1:7
	ds_write2st64_b32 v9, v74, v75 offset0:22 offset1:23
	ds_write2st64_b32 v9, v92, v93 offset0:8 offset1:9
	ds_write2st64_b32 v9, v76, v77 offset0:24 offset1:25
	ds_write2st64_b32 v9, v94, v95 offset0:10 offset1:11
	ds_write2st64_b32 v9, v78, v79 offset0:26 offset1:27
	ds_write2st64_b32 v9, v96, v97 offset0:12 offset1:13
	ds_write2st64_b32 v9, v80, v81 offset0:28 offset1:29
	ds_write2st64_b32 v9, v98, v99 offset0:14 offset1:15
	ds_write2st64_b32 v9, v82, v83 offset0:30 offset1:31
	ds_write2st64_b32 v9, v100, v101 offset0:16 offset1:17
	ds_write2st64_b32 v9, v84, v85 offset0:32 offset1:33
	v_add_u32_e32 v66, s4, v173
	s_waitcnt lgkmcnt(0)
	s_barrier
	ds_read2st64_b32 v[10:11], v66 offset1:1
	ds_read2st64_b32 v[12:13], v66 offset0:2 offset1:3
	ds_read2st64_b32 v[14:15], v66 offset0:4 offset1:5
	ds_read2st64_b32 v[38:39], v66 offset0:6 offset1:7
	v_max_f32_e32 v40, v146, v146
	s_waitcnt lgkmcnt(3)
	v_max_f32_e32 v9, v10, v10
	v_max_f32_e32 v9, v40, v9
	v_sub_f32_e32 v40, v146, v9
	v_sub_f32_e32 v9, v10, v9
	v_exp_f32_e32 v40, v40
	v_exp_f32_e32 v41, v9
	v_mov_b32_e32 v9, v11
	v_pk_mul_f32 v[8:9], v[8:9], v[40:41]
	s_nop 0
	v_add_f32_e32 v8, v8, v9
	v_div_scale_f32 v9, s[4:5], v8, v8, 1.0
	v_rcp_f32_e32 v10, v9
	s_nop 0
	v_fma_f32 v11, -v9, v10, 1.0
	v_fmac_f32_e32 v10, v11, v10
	v_div_scale_f32 v11, vcc, 1.0, v8, 1.0
	v_mul_f32_e32 v42, v11, v10
	v_fma_f32 v43, -v9, v42, v11
	v_fmac_f32_e32 v42, v43, v10
	v_fma_f32 v9, -v9, v42, v11
	v_div_fmas_f32 v9, v9, v10, v42
	v_div_fixup_f32 v9, v9, v8, 1.0
	v_mul_f32_e32 v8, v40, v9
	v_mul_f32_e32 v10, v41, v9
	ds_read2st64_b32 v[40:41], v66 offset0:18 offset1:19
	ds_read2st64_b32 v[42:43], v66 offset0:20 offset1:21
	ds_read2st64_b32 v[44:45], v66 offset0:22 offset1:23
	ds_read2st64_b32 v[46:47], v66 offset0:16 offset1:17
	s_waitcnt lgkmcnt(6)
	v_pk_mul_f32 v[12:13], v[10:11], v[12:13] op_sel_hi:[0,1]
	s_waitcnt lgkmcnt(5)
	v_pk_mul_f32 v[14:15], v[10:11], v[14:15] op_sel_hi:[0,1]
	s_waitcnt lgkmcnt(4)
	v_pk_mul_f32 v[38:39], v[10:11], v[38:39] op_sel_hi:[0,1]
	s_waitcnt lgkmcnt(3)
	v_pk_mul_f32 v[40:41], v[10:11], v[40:41] op_sel_hi:[0,1]
	v_pk_fma_f32 v[48:49], v[8:9], v[70:71], v[40:41] op_sel_hi:[0,1,1]
	s_waitcnt lgkmcnt(2)
	v_pk_mul_f32 v[40:41], v[10:11], v[42:43] op_sel_hi:[0,1]
	v_pk_fma_f32 v[50:51], v[8:9], v[72:73], v[40:41] op_sel_hi:[0,1,1]
	s_waitcnt lgkmcnt(1)
	v_pk_mul_f32 v[40:41], v[10:11], v[44:45] op_sel_hi:[0,1]
	v_pk_fma_f32 v[52:53], v[8:9], v[74:75], v[40:41] op_sel_hi:[0,1,1]
	ds_read2st64_b32 v[40:41], v66 offset0:8 offset1:9
	ds_read2st64_b32 v[42:43], v66 offset0:24 offset1:25
	ds_read2st64_b32 v[44:45], v66 offset0:10 offset1:11
	ds_read2st64_b32 v[54:55], v66 offset0:12 offset1:13
	ds_read2st64_b32 v[56:57], v66 offset0:14 offset1:15
	ds_read2st64_b32 v[58:59], v66 offset0:26 offset1:27
	ds_read2st64_b32 v[60:61], v66 offset0:28 offset1:29
	ds_read2st64_b32 v[62:63], v66 offset0:30 offset1:31
	s_waitcnt lgkmcnt(6)
	v_pk_mul_f32 v[42:43], v[10:11], v[42:43] op_sel_hi:[0,1]
	v_pk_fma_f32 v[64:65], v[8:9], v[76:77], v[42:43] op_sel_hi:[0,1,1]
	s_waitcnt lgkmcnt(5)
	v_pk_mul_f32 v[42:43], v[10:11], v[44:45] op_sel_hi:[0,1]
	s_waitcnt lgkmcnt(2)
	v_pk_mul_f32 v[44:45], v[10:11], v[58:59] op_sel_hi:[0,1]
	v_pk_fma_f32 v[58:59], v[8:9], v[78:79], v[44:45] op_sel_hi:[0,1,1]
	v_pk_mul_f32 v[44:45], v[10:11], v[54:55] op_sel_hi:[0,1]
	s_waitcnt lgkmcnt(1)
	v_pk_mul_f32 v[54:55], v[10:11], v[60:61] op_sel_hi:[0,1]
	ds_read2st64_b32 v[60:61], v66 offset0:32 offset1:33
	s_waitcnt vmcnt(0)
	v_pk_mul_f32 v[40:41], v[10:11], v[40:41] op_sel_hi:[0,1]
	v_cvt_pk_bf16_f32 v0, v208, v209
	v_cvt_pk_bf16_f32 v1, v210, v211
	v_cvt_pk_bf16_f32 v2, v212, v213
	v_cvt_pk_bf16_f32 v3, v214, v215
	v_pk_fma_f32 v[12:13], v[8:9], v[86:87], v[12:13] op_sel_hi:[0,1,1]
	v_pk_fma_f32 v[14:15], v[8:9], v[88:89], v[14:15] op_sel_hi:[0,1,1]
	v_pk_fma_f32 v[38:39], v[8:9], v[90:91], v[38:39] op_sel_hi:[0,1,1]
	v_pk_fma_f32 v[40:41], v[8:9], v[92:93], v[40:41] op_sel_hi:[0,1,1]
	v_pk_mul_f32 v[56:57], v[10:11], v[56:57] op_sel_hi:[0,1]
	s_waitcnt lgkmcnt(1)
	v_pk_mul_f32 v[62:63], v[10:11], v[62:63] op_sel_hi:[0,1]
	v_pk_mul_f32 v[46:47], v[10:11], v[46:47] op_sel_hi:[0,1]
	s_waitcnt lgkmcnt(0)
	v_pk_mul_f32 v[10:11], v[10:11], v[60:61] op_sel_hi:[0,1]
	v_cvt_pk_bf16_f32 v4, v12, v13
	v_cvt_pk_bf16_f32 v5, v14, v15
	v_cvt_pk_bf16_f32 v6, v38, v39
	v_cvt_pk_bf16_f32 v7, v40, v41
	v_pk_fma_f32 v[42:43], v[8:9], v[94:95], v[42:43] op_sel_hi:[0,1,1]
	v_pk_fma_f32 v[44:45], v[8:9], v[96:97], v[44:45] op_sel_hi:[0,1,1]
	v_pk_fma_f32 v[54:55], v[8:9], v[80:81], v[54:55] op_sel_hi:[0,1,1]
	v_pk_fma_f32 v[56:57], v[8:9], v[98:99], v[56:57] op_sel_hi:[0,1,1]
	v_pk_fma_f32 v[62:63], v[8:9], v[82:83], v[62:63] op_sel_hi:[0,1,1]
	v_pk_fma_f32 v[46:47], v[8:9], v[100:101], v[46:47] op_sel_hi:[0,1,1]
	v_pk_fma_f32 v[60:61], v[8:9], v[84:85], v[10:11] op_sel_hi:[0,1,1]
	v_mfma_f32_32x32x16_bf16 v[0:15], v[0:3], v[4:7], 0
	v_cvt_pk_bf16_f32 v42, v42, v43
	v_cvt_pk_bf16_f32 v38, v216, v217
	v_cvt_pk_bf16_f32 v39, v218, v219
	v_cvt_pk_bf16_f32 v40, v220, v221
	v_cvt_pk_bf16_f32 v41, v222, v223
	v_cvt_pk_bf16_f32 v43, v44, v45
	v_cvt_pk_bf16_f32 v44, v56, v57
	v_cvt_pk_bf16_f32 v45, v46, v47
	s_nop 1
	v_mfma_f32_32x32x16_bf16 v[0:15], v[38:41], v[42:45], v[0:15]
	v_cvt_pk_bf16_f32 v38, v224, v225
	v_cvt_pk_bf16_f32 v39, v226, v227
	v_cvt_pk_bf16_f32 v40, v228, v229
	v_cvt_pk_bf16_f32 v41, v230, v231
	v_cvt_pk_bf16_f32 v42, v48, v49
	v_cvt_pk_bf16_f32 v43, v50, v51
	v_cvt_pk_bf16_f32 v44, v52, v53
	v_cvt_pk_bf16_f32 v45, v64, v65
	v_cvt_pk_bf16_f32 v32, v232, v233
	v_cvt_pk_bf16_f32 v33, v234, v235
	v_mfma_f32_32x32x16_bf16 v[0:15], v[38:41], v[42:45], v[0:15]
	v_cvt_pk_bf16_f32 v34, v236, v237
	v_cvt_pk_bf16_f32 v35, v238, v239
	v_cvt_pk_bf16_f32 v38, v58, v59
	v_add_f32_e32 v42, 1.0, v205
	v_div_scale_f32 v43, s[4:5], v42, v42, 1.0
	v_rcp_f32_e32 v44, v43
	v_cvt_pk_bf16_f32 v39, v54, v55
	v_cvt_pk_bf16_f32 v40, v62, v63
	v_cvt_pk_bf16_f32 v41, v60, v61
	s_lshl_b32 s4, s28, 8
	s_or_b32 s4, s4, s12
	v_mfma_f32_32x32x16_bf16 v[0:15], v[32:35], v[38:41], v[0:15]
	v_fma_f32 v32, -v43, v44, 1.0
	v_fmac_f32_e32 v44, v32, v44
	v_div_scale_f32 v32, vcc, 1.0, v42, 1.0
	s_add_i32 s0, s4, s0
	v_mul_f32_e32 v33, v32, v44
	s_lshl_b64 s[0:1], s[0:1], 14
	v_fma_f32 v34, -v43, v33, v32
	s_add_u32 s0, s10, s0
	v_fmac_f32_e32 v33, v34, v44
	s_addc_u32 s1, s11, s1
	v_fma_f32 v32, -v43, v33, v32
	s_add_u32 s0, s0, s2
	v_div_fmas_f32 v32, v32, v44, v33
	s_addc_u32 s1, s1, s3
	v_add_f32_e32 v0, v0, v240
	v_div_fixup_f32 v34, v32, v42, 1.0
	v_add_u32_e32 v32, v36, v122
	v_fmac_f32_e32 v124, v205, v0
	v_mul_f32_e32 v0, v34, v124
	global_store_dword v32, v0, s[0:1] sc1
	v_add_f32_e32 v0, v1, v241
	v_fmac_f32_e32 v125, v205, v0
	v_add_u32_e32 v0, 0x4000, v32
	v_mul_f32_e32 v28, v34, v125
	global_store_dword v0, v28, s[0:1] sc1
	v_add_f32_e32 v0, v2, v242
	v_fmac_f32_e32 v126, v205, v0
	v_add_u32_e32 v0, 0x8000, v32
	v_mul_f32_e32 v2, v34, v126
	global_store_dword v0, v2, s[0:1] sc1
	v_add_f32_e32 v0, v3, v243
	v_fmac_f32_e32 v127, v205, v0
	v_add_u32_e32 v0, 0xc000, v32
	v_mul_f32_e32 v2, v34, v127
	global_store_dword v0, v2, s[0:1] sc1
	v_add_f32_e32 v0, v4, v244
	v_fmac_f32_e32 v128, v205, v0
	v_add_u32_e32 v0, 0x20000, v32
	v_mul_f32_e32 v2, v34, v128
	global_store_dword v0, v2, s[0:1] sc1
	v_add_f32_e32 v0, v5, v245
	v_fmac_f32_e32 v129, v205, v0
	v_add_u32_e32 v0, 0x24000, v32
	v_mul_f32_e32 v2, v34, v129
	global_store_dword v0, v2, s[0:1] sc1
	v_add_f32_e32 v0, v6, v246
	v_fmac_f32_e32 v130, v205, v0
	v_add_u32_e32 v0, 0x28000, v32
	v_mul_f32_e32 v2, v34, v130
	global_store_dword v0, v2, s[0:1] sc1
	v_add_f32_e32 v0, v7, v247
	v_fmac_f32_e32 v131, v205, v0
	v_add_u32_e32 v0, 0x2c000, v32
	v_mul_f32_e32 v2, v34, v131
	global_store_dword v0, v2, s[0:1] sc1
	v_add_f32_e32 v0, v8, v248
	v_fmac_f32_e32 v132, v205, v0
	v_add_u32_e32 v0, 0x40000, v32
	v_mul_f32_e32 v2, v34, v132
	global_store_dword v0, v2, s[0:1] sc1
	v_add_f32_e32 v0, v9, v249
	v_fmac_f32_e32 v133, v205, v0
	v_add_u32_e32 v0, 0x44000, v32
	v_mul_f32_e32 v2, v34, v133
	global_store_dword v0, v2, s[0:1] sc1
	v_add_f32_e32 v0, v10, v250
	v_fmac_f32_e32 v134, v205, v0
	v_add_u32_e32 v0, 0x48000, v32
	v_mul_f32_e32 v2, v34, v134
	global_store_dword v0, v2, s[0:1] sc1
	v_add_f32_e32 v0, v11, v251
	v_fmac_f32_e32 v135, v205, v0
	v_add_u32_e32 v0, 0x4c000, v32
	v_mul_f32_e32 v2, v34, v135
	global_store_dword v0, v2, s[0:1] sc1
	v_add_f32_e32 v0, v12, v252
	v_fmac_f32_e32 v136, v205, v0
	v_add_u32_e32 v0, 0x60000, v32
	v_mul_f32_e32 v2, v34, v136
	global_store_dword v0, v2, s[0:1] sc1
	v_add_f32_e32 v0, v13, v253
	v_fmac_f32_e32 v137, v205, v0
	v_add_u32_e32 v0, 0x64000, v32
	v_mul_f32_e32 v2, v34, v137
	global_store_dword v0, v2, s[0:1] sc1
	v_add_f32_e32 v0, v14, v254
	v_fmac_f32_e32 v138, v205, v0
	v_add_u32_e32 v0, 0x68000, v32
	v_mul_f32_e32 v2, v34, v138
	global_store_dword v0, v2, s[0:1] sc1
	v_add_f32_e32 v0, v15, v255
	v_fmac_f32_e32 v139, v205, v0
	v_add_u32_e32 v0, 0x6c000, v32
	v_mul_f32_e32 v2, v34, v139
	global_store_dword v0, v2, s[0:1] sc1
	s_endpgm
